# phase 3 rewritten with 16x16x32 MFMAs in two query halves: first half's stores issue under the second half's MFMAs; Wv fragments relaid out in prep for the 16-row operand with the conflict-free k-grou
# speedup vs baseline: 1.0135x; 1.0135x over previous
.Lt0_skip:
	s_movk_i32 s8, 0x80
	v_cmp_gt_u32_e32 vcc, s8, v0
	s_and_saveexec_b64 s[8:9], vcc
	s_cbranch_execz .LBB0_32
	s_load_dwordx2 s[10:11], s[0:1], 0x20
	s_waitcnt lgkmcnt(0)
	s_lshl_b32 s12, s2, 7
	s_add_i32 s12, s12, 0xffff6000
	v_or_b32_e32 v1, s12, v0
	v_lshrrev_b32_e32 v2, 5, v1
	v_lshlrev_b32_e32 v12, 3, v0
	v_and_b32_e32 v6, 0xf8, v12
	v_lshlrev_b32_e32 v2, 8, v2
	v_mov_b32_e32 v3, 0
	v_lshl_add_u64 v[4:5], v[2:3], 2, s[10:11]
	v_lshlrev_b32_e32 v2, 2, v6
	v_lshl_add_u64 v[10:11], v[4:5], 0, v[2:3]
	global_load_dwordx4 v[2:5], v[10:11], off offset:16
	global_load_dwordx4 v[6:9], v[10:11], off
	s_lshl_b32 s12, s2, 1
	s_load_dwordx2 s[10:11], s[0:1], 0x40
	s_and_b32 s12, s12, 0x70
	v_bfe_u32 v11, v12, 4, 4
	v_lshlrev_b32_e32 v10, 5, v0
	v_or_b32_e32 v11, s12, v11
	v_and_b32_e32 v10, 32, v10
	v_lshlrev_b32_e32 v11, 6, v11
	v_bfe_u32 v1, v1, 5, 5
	v_or3_b32 v1, v11, v1, v10
	v_lshlrev_b32_e32 v1, 4, v1
	s_waitcnt vmcnt(1)
	v_cvt_pk_f16_f32 v5, v4, v5
	v_cvt_pk_f16_f32 v4, v2, v3
	s_waitcnt vmcnt(0)
	v_cvt_pk_f16_f32 v3, v8, v9
	v_cvt_pk_f16_f32 v2, v6, v7
	s_lshl_b32 s13, s2, 7
	s_add_i32 s13, s13, 0xffff6000
	v_or_b32_e32 v13, s13, v0
	v_lshrrev_b32_e32 v14, 5, v13
	v_and_b32_e32 v15, 31, v13
	v_lshrrev_b32_e32 v16, 4, v14
	v_and_b32_e32 v17, 15, v14
	v_lshrrev_b32_e32 v18, 2, v15
	v_and_b32_e32 v19, 1, v15
	v_bfe_u32 v20, v15, 1, 1
	v_xor_b32_e32 v19, v19, v20
	v_lshl_or_b32 v19, v19, 1, v20
	v_lshl_or_b32 v16, v16, 9, v17
	v_lshl_or_b32 v16, v18, 6, v16
	v_lshl_or_b32 v16, v19, 4, v16
	v_lshlrev_b32_e32 v1, 4, v16
	v_and_b32_e32 v1, 0x1fff0, v1
	s_waitcnt lgkmcnt(0)
	global_store_dwordx4 v1, v[2:5], s[10:11]

.LBB1_4:
	s_or_b64 exec, exec, s[4:5]
	v_lshl_or_b32 v4, v27, 1, v96
	v_lshl_or_b32 v3, v4, 7, v3
	v_or_b32_e32 v5, 0x23600, v3
	v_or_b32_e32 v3, 0x23640, v3
	s_waitcnt lgkmcnt(0)
	s_barrier
	ds_read_b32 v5, v5
	ds_read_b32 v3, v3
	v_mad_u32_u24 v4, v4, s7, v13
	v_lshl_add_u32 v4, v119, 4, v4
	v_or_b32_e32 v6, 0x20000, v4
	ds_read_b128 v[16:19], v6
	s_waitcnt lgkmcnt(1)
	v_add_f32_e32 v3, v5, v3
	v_add_u32_e32 v5, 0x20020, v4
	v_add_u32_e32 v6, 0x20040, v4
	ds_read_b128 v[112:115], v5
	ds_read_b128 v[108:111], v6
	v_add_u32_e32 v5, 0x20060, v4
	v_add_u32_e32 v6, 0x20080, v4
	v_lshlrev_b32_e32 v7, 1, v101
	ds_read_b128 v[104:107], v5
	ds_read_b128 v[96:99], v6
	v_lshrrev_b32_e32 v5, 2, v100
	v_or_b32_e32 v6, v28, v125
	v_and_b32_e32 v7, 2, v7
	v_bfe_u32 v8, v0, 1, 1
	v_and_b32_e32 v164, 8, v121
	v_bfe_i32 v9, v0, 7, 1
	v_or3_b32 v8, v8, v7, v164
	v_and_b32_e32 v0, 12, v0
	v_add_lshl_u32 v10, v6, v5, 8
	v_or_b32_e32 v5, v6, v5
	v_and_b32_e32 v9, 0xc000, v9
	v_lshlrev_b32_e32 v12, 8, v5
	v_bitop3_b32 v5, v0, v8, v124 bitop3:0x36
	v_lshl_or_b32 v13, v5, 4, v9
	v_bitop3_b32 v6, v0, v8, v2 bitop3:0x36
	v_or_b32_e32 v15, 0x1000, v12
	v_lshl_or_b32 v14, v6, 4, v9
	v_add_u32_e32 v7, v13, v15
	v_or_b32_e32 v24, 0x1400, v12
	v_or_b32_e32 v20, v7, v1
	v_add_u32_e32 v7, v14, v24
	v_add_u32_e32 v25, 0x2000, v10
	v_add_u32_e32 v5, v13, v12
	v_add_u32_e32 v6, v14, v12
	v_or_b32_e32 v22, v7, v1
	v_add_u32_e32 v7, v13, v25
	v_add_u32_e32 v150, 0x3000, v10
	v_or_b32_e32 v8, 4, v8
	v_add_u32_e32 v4, 0x200a0, v4
	v_or_b32_e32 v5, v5, v1
	v_or_b32_e32 v6, v6, v1
	v_or_b32_e32 v27, v7, v1
	v_add_u32_e32 v31, v13, v150
	v_add_u32_e32 v151, 0x3400, v10
	v_bitop3_b32 v124, v0, v8, v124 bitop3:0x36
	v_bitop3_b32 v0, v0, v8, v2 bitop3:0x36
	ds_read_b128 v[100:103], v4
	ds_read_b64_tr_b16 v[4:5], v5
	ds_read_b64_tr_b16 v[6:7], v6 offset:1024
	ds_read_b64_tr_b16 v[20:21], v20
	ds_read_b64_tr_b16 v[22:23], v22
	ds_read_b64_tr_b16 v[28:29], v27
	v_add_u32_e32 v27, 0x2400, v10
	v_or_b32_e32 v128, v31, v1
	v_add_u32_e32 v31, v14, v151
	v_add_u32_e32 v152, 0x4000, v10
	v_add_u32_e32 v158, 0x4400, v10
	v_lshl_or_b32 v124, v124, 4, v9
	v_lshl_or_b32 v0, v0, 4, v9
	v_add_u32_e32 v11, 0x5000, v10
	v_add_u32_e32 v30, v14, v27
	v_or_b32_e32 v130, v31, v1
	v_add_u32_e32 v31, v13, v152
	v_add_u32_e32 v134, v14, v158
	v_add_u32_e32 v10, 0x5400, v10
	v_add_u32_e32 v135, v124, v12
	v_add_u32_e32 v2, v0, v12
	v_add_u32_e32 v8, v124, v15
	v_or_b32_e32 v30, v30, v1
	v_or_b32_e32 v132, v31, v1
	v_or_b32_e32 v134, v134, v1
	v_add_u32_e32 v13, v13, v11
	v_add_u32_e32 v14, v14, v10
	v_or_b32_e32 v140, v135, v1
	v_or_b32_e32 v2, v2, v1
	v_or_b32_e32 v8, v8, v1
	v_add_u32_e32 v9, v0, v24
	v_add_u32_e32 v12, v124, v25
	ds_read_b64_tr_b16 v[30:31], v30
	ds_read_b64_tr_b16 v[128:129], v128
	ds_read_b64_tr_b16 v[130:131], v130
	ds_read_b64_tr_b16 v[132:133], v132
	v_or_b32_e32 v13, v13, v1
	v_or_b32_e32 v14, v14, v1
	ds_read_b64_tr_b16 v[134:135], v134
	ds_read_b64_tr_b16 v[136:137], v13
	ds_read_b64_tr_b16 v[138:139], v14
	ds_read_b64_tr_b16 v[140:141], v140
	v_or_b32_e32 v9, v9, v1
	v_or_b32_e32 v12, v12, v1
	ds_read_b64_tr_b16 v[142:143], v2 offset:1024
	ds_read_b64_tr_b16 v[144:145], v8
	ds_read_b64_tr_b16 v[146:147], v9
	ds_read_b64_tr_b16 v[148:149], v12
	v_add_u32_e32 v2, v0, v27
	v_add_u32_e32 v8, v124, v150
	v_or_b32_e32 v2, v2, v1
	v_or_b32_e32 v8, v8, v1
	v_add_u32_e32 v9, v0, v151
	v_add_u32_e32 v12, v124, v152
	v_or_b32_e32 v9, v9, v1
	v_or_b32_e32 v12, v12, v1
	ds_read_b64_tr_b16 v[150:151], v2
	ds_read_b64_tr_b16 v[152:153], v8
	ds_read_b64_tr_b16 v[154:155], v9
	ds_read_b64_tr_b16 v[156:157], v12
	v_add_u32_e32 v2, v0, v158
	v_add_u32_e32 v8, v124, v11
	v_add_u32_e32 v0, v0, v10
	v_or_b32_e32 v2, v2, v1
	v_or_b32_e32 v8, v8, v1
	v_or_b32_e32 v0, v0, v1
	v_div_scale_f32 v1, s[8:9], v3, v3, 1.0
	v_rcp_f32_e32 v9, v1
	ds_read_b64_tr_b16 v[158:159], v2
	ds_read_b64_tr_b16 v[160:161], v8
	ds_read_b64_tr_b16 v[162:163], v0
	s_mov_b32 s4, 0xc000
	s_movk_i32 s5, 0x4000
	v_fma_f32 v0, -v1, v9, 1.0
	v_fmac_f32_e32 v9, v0, v9
	v_div_scale_f32 v0, vcc, 1.0, v3, 1.0
	v_mul_f32_e32 v2, v0, v9
	v_fma_f32 v8, -v1, v2, v0
	v_fmac_f32_e32 v2, v8, v9
	v_fma_f32 v0, -v1, v2, v0
	v_div_fmas_f32 v0, v0, v9, v2
	v_div_fixup_f32 v124, v0, v3, 1.0
	s_waitcnt lgkmcnt(14)
	v_mfma_f32_32x32x16_f16 v[0:15], v[4:7], v[16:19], 0
	s_mov_b32 s7, 0x18000
	v_lshlrev_b32_e32 v172, 2, v126
	v_mov_b32_e32 v173, 0
	v_mfma_f32_32x32x16_f16 v[0:15], v[20:23], v[112:115], v[0:15]
	v_or_b32_e32 v20, v26, v116
	v_and_b32_e32 v21, 0x4000, v118
	v_lshl_or_b32 v20, v20, 8, v21
	v_bitop3_b32 v118, v121, v120, 8 bitop3:0x6c
	v_or3_b32 v121, v20, v125, s7
	v_mfma_f32_32x32x16_f16 v[0:15], v[28:31], v[108:111], v[0:15]
	v_mfma_f32_32x32x16_f16 v[0:15], v[128:131], v[104:107], v[0:15]
	v_mfma_f32_32x32x16_f16 v[0:15], v[132:135], v[96:99], v[0:15]
	s_waitcnt lgkmcnt(12)
	v_mfma_f32_32x32x16_f16 v[0:15], v[136:139], v[100:103], v[0:15]
	s_nop 11
	v_fma_mixlo_f16 v20, v124, v0, 0
	v_mov_b32_e32 v0, v1
	v_mov_b32_e32 v1, v2
	v_pk_mul_f32 v[0:1], v[124:125], v[0:1] op_sel_hi:[0,1]
	v_cvt_pk_f16_f32 v1, v0, v1
	v_pack_b32_f16 v0, v20, v1
	s_waitcnt lgkmcnt(10)
	v_mfma_f32_32x32x16_f16 v[16:31], v[140:143], v[16:19], 0
	v_fma_mixlo_f16 v2, v124, v3, 0
	v_alignbit_b32 v1, v2, v1, 16
	v_lshl_or_b32 v2, v118, 4, v121
	ds_write_b64 v2, v[0:1]
	v_mov_b32_e32 v0, v5
	v_mov_b32_e32 v1, v6
	v_pk_mul_f32 v[0:1], v[124:125], v[0:1] op_sel_hi:[0,1]
	s_waitcnt lgkmcnt(9)
	v_mfma_f32_32x32x16_f16 v[16:31], v[144:147], v[112:115], v[16:31]
	v_fma_mixlo_f16 v2, v124, v4, 0
	v_cvt_pk_f16_f32 v1, v0, v1
	v_pack_b32_f16 v0, v2, v1
	v_fma_mixlo_f16 v2, v124, v7, 0
	v_alignbit_b32 v1, v2, v1, 16
	v_bitop3_b32 v2, v164, v120, 1 bitop3:0x36
	v_lshl_or_b32 v2, v2, 4, v121
	s_waitcnt lgkmcnt(7)
	v_mfma_f32_32x32x16_f16 v[16:31], v[148:151], v[108:111], v[16:31]
	ds_write_b64 v2, v[0:1]
	v_mov_b32_e32 v0, v9
	v_mov_b32_e32 v1, v10
	v_mul_f32_e64 v0, v124, v0
	v_mul_f32_e64 v1, v124, v1
	v_fma_mixlo_f16 v2, v124, v8, 0
	v_cvt_pk_f16_f32 v1, v0, v1
	v_pack_b32_f16 v0, v2, v1
	s_waitcnt lgkmcnt(6)
	v_mfma_f32_32x32x16_f16 v[16:31], v[152:155], v[104:107], v[16:31]
	v_fma_mixlo_f16 v2, v124, v11, 0
	v_alignbit_b32 v1, v2, v1, 16
	v_bitop3_b32 v2, v164, v120, 2 bitop3:0x36
	v_lshl_or_b32 v2, v2, 4, v121
	ds_write_b64 v2, v[0:1]
	v_mov_b32_e32 v0, v13
	v_mov_b32_e32 v1, v14
	s_waitcnt lgkmcnt(5)
	v_mfma_f32_32x32x16_f16 v[16:31], v[156:159], v[96:99], v[16:31]
	v_mul_f32_e64 v0, v124, v0
	v_mul_f32_e64 v1, v124, v1
	v_fma_mixlo_f16 v2, v124, v12, 0
	v_cvt_pk_f16_f32 v1, v0, v1
	v_pack_b32_f16 v0, v2, v1
	v_fma_mixlo_f16 v2, v124, v15, 0
	v_alignbit_b32 v1, v2, v1, 16
	v_bitop3_b32 v2, v164, v120, 3 bitop3:0x36
	s_waitcnt lgkmcnt(3)
	v_mfma_f32_32x32x16_f16 v[16:31], v[160:163], v[100:103], v[16:31]
	v_lshl_or_b32 v2, v2, 4, v121
	ds_write_b64 v2, v[0:1]
	s_nop 9
	v_mov_b32_e32 v0, v17
	v_mov_b32_e32 v1, v18
	v_pk_mul_f32 v[0:1], v[124:125], v[0:1] op_sel_hi:[0,1]
	v_fma_mixlo_f16 v2, v124, v16, 0
	v_cvt_pk_f16_f32 v1, v0, v1
	v_pack_b32_f16 v0, v2, v1
	v_fma_mixlo_f16 v2, v124, v19, 0
	v_alignbit_b32 v1, v2, v1, 16
	v_bitop3_b32 v2, v164, v120, 4 bitop3:0x36
	v_lshl_or_b32 v2, v2, 4, v121
	ds_write_b64 v2, v[0:1]
	v_mov_b32_e32 v0, v21
	v_mov_b32_e32 v1, v22
	v_pk_mul_f32 v[0:1], v[124:125], v[0:1] op_sel_hi:[0,1]
	v_fma_mixlo_f16 v2, v124, v20, 0
	v_cvt_pk_f16_f32 v1, v0, v1
	v_pack_b32_f16 v0, v2, v1
	v_fma_mixlo_f16 v2, v124, v23, 0
	v_alignbit_b32 v1, v2, v1, 16
	v_bitop3_b32 v2, v164, v120, 5 bitop3:0x36
	v_lshl_or_b32 v2, v2, 4, v121
	ds_write_b64 v2, v[0:1]
	v_mov_b32_e32 v0, v25
	v_mov_b32_e32 v1, v26
	v_pk_mul_f32 v[0:1], v[124:125], v[0:1] op_sel_hi:[0,1]
	v_fma_mixlo_f16 v2, v124, v24, 0
	v_cvt_pk_f16_f32 v1, v0, v1
	v_pack_b32_f16 v0, v2, v1
	v_fma_mixlo_f16 v2, v124, v27, 0
	v_alignbit_b32 v1, v2, v1, 16
	v_bitop3_b32 v2, v164, v120, 6 bitop3:0x36
	v_lshl_or_b32 v2, v2, 4, v121
	ds_write_b64 v2, v[0:1]
	v_mov_b32_e32 v0, v29
	v_mov_b32_e32 v1, v30
	v_pk_mul_f32 v[0:1], v[124:125], v[0:1] op_sel_hi:[0,1]
	v_fma_mixlo_f16 v2, v124, v28, 0
	v_cvt_pk_f16_f32 v1, v0, v1
	v_pack_b32_f16 v0, v2, v1
	v_fma_mixlo_f16 v2, v124, v31, 0
	v_alignbit_b32 v1, v2, v1, 16
	v_bitop3_b32 v2, v164, v120, 7 bitop3:0x36
	v_lshl_or_b32 v2, v2, 4, v121
	ds_write_b64 v2, v[0:1]
	v_lshl_add_u64 v[0:1], s[0:1], 0, v[172:173]
	v_lshlrev_b32_e32 v172, 2, v127
	v_lshl_add_u64 v[0:1], v[0:1], 0, v[172:173]
	s_waitcnt lgkmcnt(0)
	s_barrier
	v_and_b32_e32 v245, 15, v116
	v_lshrrev_b32_e32 v246, 4, v116
	v_lshl_or_b32 v246, v119, 1, v246
	v_lshrrev_b32_e32 v250, 5, v126
	v_and_b32_e32 v250, 7, v250
	v_and_b32_e32 v247, 1, v246
	v_lshrrev_b32_e32 v248, 1, v246
	v_xor_b32_e32 v248, v248, v247
	v_lshl_or_b32 v247, v247, 1, v248
	v_and_b32_e32 v248, 3, v245
	v_lshrrev_b32_e32 v249, 2, v245
	v_lshl_or_b32 v248, v248, 2, v249
	v_xor_b32_e32 v247, v247, v248
	v_lshlrev_b32_e32 v240, 8, v245
	v_lshl_or_b32 v240, v247, 4, v240
	v_add_u32_e32 v240, 0x18000, v240
	v_xor_b32_e32 v241, 64, v240
	v_xor_b32_e32 v242, 0x80, v240
	v_xor_b32_e32 v243, 0xc0, v240
	v_lshlrev_b32_e32 v249, 7, v250
	v_lshl_or_b32 v249, v246, 4, v249
	v_and_b32_e32 v249, 0x3f0, v249
	global_load_dwordx4 v[96:99], v249, s[0:1]
	global_load_dwordx4 v[100:103], v249, s[0:1] offset:64
	v_lshlrev_b32_e32 v244, 19, v250
	v_lshl_or_b32 v244, v246, 16, v244
	v_lshl_or_b32 v244, v245, 3, v244
	v_and_b32_e32 v244, 0x3fff78, v244
	s_lshl_b64 s[22:23], s[2:3], 22
	s_add_u32 s22, s22, s12
	s_addc_u32 s23, s23, s13
	s_lshl_b32 s24, s14, 3
	s_add_u32 s22, s22, s24
	s_addc_u32 s23, s23, 0
	ds_read_b128 v[112:115], v240
	ds_read_b128 v[144:147], v240 offset:8192
	ds_read_b128 v[116:119], v241
	ds_read_b128 v[148:151], v241 offset:8192
	ds_read_b128 v[120:123], v242
	ds_read_b128 v[152:155], v242 offset:8192
	ds_read_b128 v[124:127], v243
	ds_read_b128 v[156:159], v243 offset:8192
	ds_read_b128 v[128:131], v240 offset:16384
	ds_read_b128 v[160:163], v240 offset:24576
	ds_read_b128 v[132:135], v241 offset:16384
	ds_read_b128 v[164:167], v241 offset:24576
	ds_read_b128 v[136:139], v242 offset:16384
	ds_read_b128 v[168:171], v242 offset:24576
	ds_read_b128 v[140:143], v243 offset:16384
	ds_read_b128 v[172:175], v243 offset:24576
	s_waitcnt vmcnt(2)
	s_waitcnt lgkmcnt(14)
	v_mfma_f32_16x16x32_f16 v[0:3], v[36:39], v[112:115], 0
	v_mfma_f32_16x16x32_f16 v[4:7], v[36:39], v[144:147], 0
	v_mfma_f32_16x16x32_f16 v[8:11], v[76:79], v[112:115], 0
	v_mfma_f32_16x16x32_f16 v[12:15], v[76:79], v[144:147], 0
	s_waitcnt lgkmcnt(12)
	v_mfma_f32_16x16x32_f16 v[0:3], v[32:35], v[116:119], v[0:3]
	v_mfma_f32_16x16x32_f16 v[4:7], v[32:35], v[148:151], v[4:7]
	v_mfma_f32_16x16x32_f16 v[8:11], v[72:75], v[116:119], v[8:11]
	v_mfma_f32_16x16x32_f16 v[12:15], v[72:75], v[148:151], v[12:15]
	s_waitcnt lgkmcnt(10)
	v_mfma_f32_16x16x32_f16 v[0:3], v[64:67], v[120:123], v[0:3]
	v_mfma_f32_16x16x32_f16 v[4:7], v[64:67], v[152:155], v[4:7]
	v_mfma_f32_16x16x32_f16 v[8:11], v[68:71], v[120:123], v[8:11]
	v_mfma_f32_16x16x32_f16 v[12:15], v[68:71], v[152:155], v[12:15]
	s_waitcnt lgkmcnt(8)
	v_mfma_f32_16x16x32_f16 v[0:3], v[48:51], v[124:127], v[0:3]
	v_mfma_f32_16x16x32_f16 v[4:7], v[48:51], v[156:159], v[4:7]
	v_mfma_f32_16x16x32_f16 v[8:11], v[52:55], v[124:127], v[8:11]
	v_mfma_f32_16x16x32_f16 v[12:15], v[52:55], v[156:159], v[12:15]
	s_waitcnt lgkmcnt(6)
	v_mfma_f32_16x16x32_f16 v[0:3], v[92:95], v[128:131], v[0:3]
	v_mfma_f32_16x16x32_f16 v[4:7], v[92:95], v[160:163], v[4:7]
	v_mfma_f32_16x16x32_f16 v[8:11], v[60:63], v[128:131], v[8:11]
	v_mfma_f32_16x16x32_f16 v[12:15], v[60:63], v[160:163], v[12:15]
	s_waitcnt lgkmcnt(4)
	v_mfma_f32_16x16x32_f16 v[0:3], v[84:87], v[132:135], v[0:3]
	v_mfma_f32_16x16x32_f16 v[4:7], v[84:87], v[164:167], v[4:7]
	v_mfma_f32_16x16x32_f16 v[8:11], v[56:59], v[132:135], v[8:11]
	v_mfma_f32_16x16x32_f16 v[12:15], v[56:59], v[164:167], v[12:15]
	s_waitcnt lgkmcnt(2)
	v_mfma_f32_16x16x32_f16 v[0:3], v[80:83], v[136:139], v[0:3]
	v_mfma_f32_16x16x32_f16 v[4:7], v[80:83], v[168:171], v[4:7]
	v_mfma_f32_16x16x32_f16 v[8:11], v[44:47], v[136:139], v[8:11]
	v_mfma_f32_16x16x32_f16 v[12:15], v[44:47], v[168:171], v[12:15]
	s_waitcnt lgkmcnt(0)
	v_mfma_f32_16x16x32_f16 v[0:3], v[88:91], v[140:143], v[0:3]
	v_mfma_f32_16x16x32_f16 v[4:7], v[88:91], v[172:175], v[4:7]
	v_mfma_f32_16x16x32_f16 v[8:11], v[40:43], v[140:143], v[8:11]
	v_mfma_f32_16x16x32_f16 v[12:15], v[40:43], v[172:175], v[12:15]
	ds_read_b128 v[176:179], v240 offset:4096
	ds_read_b128 v[208:211], v240 offset:12288
	ds_read_b128 v[180:183], v241 offset:4096
	ds_read_b128 v[212:215], v241 offset:12288
	ds_read_b128 v[184:187], v242 offset:4096
	ds_read_b128 v[216:219], v242 offset:12288
	ds_read_b128 v[188:191], v243 offset:4096
	ds_read_b128 v[220:223], v243 offset:12288
	ds_read_b128 v[192:195], v240 offset:20480
	ds_read_b128 v[224:227], v240 offset:28672
	ds_read_b128 v[196:199], v241 offset:20480
	ds_read_b128 v[228:231], v241 offset:28672
	ds_read_b128 v[200:203], v242 offset:20480
	ds_read_b128 v[232:235], v242 offset:28672
	ds_read_b128 v[204:207], v243 offset:20480
	ds_read_b128 v[236:239], v243 offset:28672
	s_waitcnt vmcnt(0)
	s_waitcnt lgkmcnt(14)
	v_mfma_f32_16x16x32_f16 v[16:19], v[36:39], v[176:179], 0
	v_mfma_f32_16x16x32_f16 v[20:23], v[36:39], v[208:211], 0
	v_mfma_f32_16x16x32_f16 v[24:27], v[76:79], v[176:179], 0
	v_mfma_f32_16x16x32_f16 v[28:31], v[76:79], v[208:211], 0
	s_add_u32 s26, s22, 0x0
	s_addc_u32 s27, s23, 0
	v_add_f32_e32 v104, v0, v96
	v_add_f32_e32 v105, v4, v96
	global_store_dwordx2 v244, v[104:105], s[26:27] nt
	s_waitcnt lgkmcnt(12)
	v_mfma_f32_16x16x32_f16 v[16:19], v[32:35], v[180:183], v[16:19]
	v_mfma_f32_16x16x32_f16 v[20:23], v[32:35], v[212:215], v[20:23]
	v_mfma_f32_16x16x32_f16 v[24:27], v[72:75], v[180:183], v[24:27]
	v_mfma_f32_16x16x32_f16 v[28:31], v[72:75], v[212:215], v[28:31]
	s_add_u32 s26, s22, 0x4000
	s_addc_u32 s27, s23, 0
	v_add_f32_e32 v106, v1, v97
	v_add_f32_e32 v107, v5, v97
	global_store_dwordx2 v244, v[106:107], s[26:27] nt
	s_waitcnt lgkmcnt(10)
	v_mfma_f32_16x16x32_f16 v[16:19], v[64:67], v[184:187], v[16:19]
	v_mfma_f32_16x16x32_f16 v[20:23], v[64:67], v[216:219], v[20:23]
	v_mfma_f32_16x16x32_f16 v[24:27], v[68:71], v[184:187], v[24:27]
	v_mfma_f32_16x16x32_f16 v[28:31], v[68:71], v[216:219], v[28:31]
	s_add_u32 s26, s22, 0x8000
	s_addc_u32 s27, s23, 0
	v_add_f32_e32 v108, v2, v98
	v_add_f32_e32 v109, v6, v98
	global_store_dwordx2 v244, v[108:109], s[26:27] nt
	s_waitcnt lgkmcnt(8)
	v_mfma_f32_16x16x32_f16 v[16:19], v[48:51], v[188:191], v[16:19]
	v_mfma_f32_16x16x32_f16 v[20:23], v[48:51], v[220:223], v[20:23]
	v_mfma_f32_16x16x32_f16 v[24:27], v[52:55], v[188:191], v[24:27]
	v_mfma_f32_16x16x32_f16 v[28:31], v[52:55], v[220:223], v[28:31]
	s_add_u32 s26, s22, 0xc000
	s_addc_u32 s27, s23, 0
	v_add_f32_e32 v110, v3, v99
	v_add_f32_e32 v111, v7, v99
	global_store_dwordx2 v244, v[110:111], s[26:27] nt
	s_waitcnt lgkmcnt(6)
	v_mfma_f32_16x16x32_f16 v[16:19], v[92:95], v[192:195], v[16:19]
	v_mfma_f32_16x16x32_f16 v[20:23], v[92:95], v[224:227], v[20:23]
	v_mfma_f32_16x16x32_f16 v[24:27], v[60:63], v[192:195], v[24:27]
	v_mfma_f32_16x16x32_f16 v[28:31], v[60:63], v[224:227], v[28:31]
	s_add_u32 s26, s22, 0x40000
	s_addc_u32 s27, s23, 0
	v_add_f32_e32 v104, v8, v100
	v_add_f32_e32 v105, v12, v100
	global_store_dwordx2 v244, v[104:105], s[26:27] nt
	s_waitcnt lgkmcnt(4)
	v_mfma_f32_16x16x32_f16 v[16:19], v[84:87], v[196:199], v[16:19]
	v_mfma_f32_16x16x32_f16 v[20:23], v[84:87], v[228:231], v[20:23]
	v_mfma_f32_16x16x32_f16 v[24:27], v[56:59], v[196:199], v[24:27]
	v_mfma_f32_16x16x32_f16 v[28:31], v[56:59], v[228:231], v[28:31]
	s_add_u32 s26, s22, 0x44000
	s_addc_u32 s27, s23, 0
	v_add_f32_e32 v106, v9, v101
	v_add_f32_e32 v107, v13, v101
	global_store_dwordx2 v244, v[106:107], s[26:27] nt
	s_waitcnt lgkmcnt(2)
	v_mfma_f32_16x16x32_f16 v[16:19], v[80:83], v[200:203], v[16:19]
	v_mfma_f32_16x16x32_f16 v[20:23], v[80:83], v[232:235], v[20:23]
	v_mfma_f32_16x16x32_f16 v[24:27], v[44:47], v[200:203], v[24:27]
	v_mfma_f32_16x16x32_f16 v[28:31], v[44:47], v[232:235], v[28:31]
	s_add_u32 s26, s22, 0x48000
	s_addc_u32 s27, s23, 0
	v_add_f32_e32 v108, v10, v102
	v_add_f32_e32 v109, v14, v102
	global_store_dwordx2 v244, v[108:109], s[26:27] nt
	s_waitcnt lgkmcnt(0)
	v_mfma_f32_16x16x32_f16 v[16:19], v[88:91], v[204:207], v[16:19]
	v_mfma_f32_16x16x32_f16 v[20:23], v[88:91], v[236:239], v[20:23]
	v_mfma_f32_16x16x32_f16 v[24:27], v[40:43], v[204:207], v[24:27]
	v_mfma_f32_16x16x32_f16 v[28:31], v[40:43], v[236:239], v[28:31]
	s_add_u32 s26, s22, 0x4c000
	s_addc_u32 s27, s23, 0
	v_add_f32_e32 v110, v11, v103
	v_add_f32_e32 v111, v15, v103
	global_store_dwordx2 v244, v[110:111], s[26:27] nt
	s_nop 7
	s_nop 1
	s_add_u32 s26, s22, 0x0
	s_addc_u32 s27, s23, 0
	v_add_f32_e32 v104, v16, v96
	v_add_f32_e32 v105, v20, v96
	global_store_dwordx2 v244, v[104:105], s[26:27] offset:128 nt
	s_add_u32 s26, s22, 0x4000
	s_addc_u32 s27, s23, 0
	v_add_f32_e32 v106, v17, v97
	v_add_f32_e32 v107, v21, v97
	global_store_dwordx2 v244, v[106:107], s[26:27] offset:128 nt
	s_add_u32 s26, s22, 0x8000
	s_addc_u32 s27, s23, 0
	v_add_f32_e32 v108, v18, v98
	v_add_f32_e32 v109, v22, v98
	global_store_dwordx2 v244, v[108:109], s[26:27] offset:128 nt
	s_add_u32 s26, s22, 0xc000
	s_addc_u32 s27, s23, 0
	v_add_f32_e32 v110, v19, v99
	v_add_f32_e32 v111, v23, v99
	global_store_dwordx2 v244, v[110:111], s[26:27] offset:128 nt
	s_add_u32 s26, s22, 0x40000
	s_addc_u32 s27, s23, 0
	v_add_f32_e32 v104, v24, v100
	v_add_f32_e32 v105, v28, v100
	global_store_dwordx2 v244, v[104:105], s[26:27] offset:128 nt
	s_add_u32 s26, s22, 0x44000
	s_addc_u32 s27, s23, 0
	v_add_f32_e32 v106, v25, v101
	v_add_f32_e32 v107, v29, v101
	global_store_dwordx2 v244, v[106:107], s[26:27] offset:128 nt
	s_add_u32 s26, s22, 0x48000
	s_addc_u32 s27, s23, 0
	v_add_f32_e32 v108, v26, v102
	v_add_f32_e32 v109, v30, v102
	global_store_dwordx2 v244, v[108:109], s[26:27] offset:128 nt
	s_add_u32 s26, s22, 0x4c000
	s_addc_u32 s27, s23, 0
	v_add_f32_e32 v110, v27, v103
	v_add_f32_e32 v111, v31, v103
	global_store_dwordx2 v244, v[110:111], s[26:27] offset:128 nt
	s_endpgm

	.amdhsa_kernel _Z7na_mainPKDF16_PKhS0_PKfS4_S4_S4_Pf
		.amdhsa_group_segment_fixed_size 162048
		.amdhsa_private_segment_fixed_size 0
		.amdhsa_kernarg_size 64
		.amdhsa_user_sgpr_count 2
		.amdhsa_user_sgpr_dispatch_ptr 0
		.amdhsa_user_sgpr_queue_ptr 0
		.amdhsa_user_sgpr_kernarg_segment_ptr 1
		.amdhsa_user_sgpr_dispatch_id 0
		.amdhsa_user_sgpr_kernarg_preload_length 0
		.amdhsa_user_sgpr_kernarg_preload_offset 0
		.amdhsa_user_sgpr_private_segment_size 0
		.amdhsa_uses_dynamic_stack 0
		.amdhsa_enable_private_segment 0
		.amdhsa_system_sgpr_workgroup_id_x 1
		.amdhsa_system_sgpr_workgroup_id_y 0
		.amdhsa_system_sgpr_workgroup_id_z 0
		.amdhsa_system_sgpr_workgroup_info 0
		.amdhsa_system_vgpr_workitem_id 0
		.amdhsa_next_free_vgpr 251
		.amdhsa_next_free_sgpr 96
		.amdhsa_accum_offset 252
		.amdhsa_reserve_vcc 1
		.amdhsa_float_round_mode_32 0
		.amdhsa_float_round_mode_16_64 0
		.amdhsa_float_denorm_mode_32 3
		.amdhsa_float_denorm_mode_16_64 3
		.amdhsa_dx10_clamp 1
		.amdhsa_ieee_mode 1
		.amdhsa_fp16_overflow 0
		.amdhsa_tg_split 0
		.amdhsa_exception_fp_ieee_invalid_op 0
		.amdhsa_exception_fp_denorm_src 0
		.amdhsa_exception_fp_ieee_div_zero 0
		.amdhsa_exception_fp_ieee_overflow 0
		.amdhsa_exception_fp_ieee_underflow 0
		.amdhsa_exception_fp_ieee_inexact 0
		.amdhsa_exception_int_div_zero 0
	.end_amdhsa_kernel

amdhsa.kernels:
  - .agpr_count:     16
    .args:
      - .actual_access:  read_only
        .address_space:  global
        .offset:         0
        .size:           8
        .value_kind:     global_buffer
      - .actual_access:  read_only
        .address_space:  global
        .offset:         8
        .size:           8
        .value_kind:     global_buffer
      - .actual_access:  read_only
        .address_space:  global
        .offset:         16
        .size:           8
        .value_kind:     global_buffer
      - .actual_access:  read_only
        .address_space:  global
        .offset:         24
        .size:           8
        .value_kind:     global_buffer
      - .actual_access:  read_only
        .address_space:  global
        .offset:         32
        .size:           8
        .value_kind:     global_buffer
      - .actual_access:  read_only
        .address_space:  global
        .offset:         40
        .size:           8
        .value_kind:     global_buffer
      - .actual_access:  write_only
        .address_space:  global
        .offset:         48
        .size:           8
        .value_kind:     global_buffer
      - .actual_access:  write_only
        .address_space:  global
        .offset:         56
        .size:           8
        .value_kind:     global_buffer
      - .actual_access:  write_only
        .address_space:  global
        .offset:         64
        .size:           8
        .value_kind:     global_buffer
      - .actual_access:  write_only
        .address_space:  global
        .offset:         72
        .size:           8
        .value_kind:     global_buffer
      - .actual_access:  write_only
        .address_space:  global
        .offset:         80
        .size:           8
        .value_kind:     global_buffer
      - .actual_access:  write_only
        .address_space:  global
        .offset:         88
        .size:           8
        .value_kind:     global_buffer
    .group_segment_fixed_size: 50176
    .kernarg_segment_align: 8
    .kernarg_segment_size: 96
    .language:       OpenCL C
    .language_version:
      - 2
      - 0
    .max_flat_workgroup_size: 256
    .name:           _Z7na_prepPKfS0_S0_S0_S0_S0_PDF16_PhS1_PfS3_S3_
    .private_segment_fixed_size: 0
    .sgpr_count:     23
    .sgpr_spill_count: 0
    .symbol:         _Z7na_prepPKfS0_S0_S0_S0_S0_PDF16_PhS1_PfS3_S3_.kd
    .uniform_work_group_size: 1
    .uses_dynamic_stack: false
    .vgpr_count:     116
    .vgpr_spill_count: 0
    .wavefront_size: 64
  - .agpr_count:     0
    .args:
      - .address_space:  global
        .offset:         0
        .size:           8
        .value_kind:     global_buffer
      - .actual_access:  read_only
        .address_space:  global
        .offset:         8
        .size:           8
        .value_kind:     global_buffer
      - .actual_access:  read_only
        .address_space:  global
        .offset:         16
        .size:           8
        .value_kind:     global_buffer
      - .actual_access:  read_only
        .address_space:  global
        .offset:         24
        .size:           8
        .value_kind:     global_buffer
      - .actual_access:  read_only
        .address_space:  global
        .offset:         32
        .size:           8
        .value_kind:     global_buffer
      - .actual_access:  read_only
        .address_space:  global
        .offset:         40
        .size:           8
        .value_kind:     global_buffer
      - .actual_access:  read_only
        .address_space:  global
        .offset:         48
        .size:           8
        .value_kind:     global_buffer
      - .actual_access:  write_only
        .address_space:  global
        .offset:         56
        .size:           8
        .value_kind:     global_buffer
    .group_segment_fixed_size: 162048
    .kernarg_segment_align: 8
    .kernarg_segment_size: 64
    .language:       OpenCL C
    .language_version:
      - 2
      - 0
    .max_flat_workgroup_size: 512
    .name:           _Z7na_mainPKDF16_PKhS0_PKfS4_S4_S4_Pf
    .private_segment_fixed_size: 0
    .sgpr_count:     24
    .sgpr_spill_count: 0
    .symbol:         _Z7na_mainPKDF16_PKhS0_PKfS4_S4_S4_Pf.kd
    .uniform_work_group_size: 1
    .uses_dynamic_stack: false
    .vgpr_count:     251
    .vgpr_spill_count: 0
    .wavefront_size: 64
